# mixer: output row addresses advanced incrementally per chunk
# baseline (speedup 1.0000x reference)
.LBB0_464:
	s_ashr_i32 s8, s24, 2
	s_add_i32 s24, s8, s78
	s_lshl_b32 s8, s79, 7
	s_and_b64 s[78:79], s[76:77], exec
	s_movk_i32 s9, 0x1500
	s_cselect_b32 s9, s9, 0x1800
	s_and_b64 s[6:7], exec, s[6:7]
	s_cselect_b32 s6, 0x900, s9
	s_lshl_b32 s2, s2, 6
	s_and_b32 s40, s2, 64
	s_add_i32 s7, s81, s8
	s_or_b32 s78, s7, s40
	s_ashr_i32 s7, s5, 31
	s_lshr_b32 s7, s7, 30
	s_add_i32 s7, s5, s7
	s_and_b32 s7, s7, 0x1ffffc
	s_sub_i32 s5, s5, s7
	s_lshl_b32 s84, s5, 11
	v_cndmask_b32_e64 v3, v111, v110, s[76:77]
	v_add_u32_e32 v3, s84, v3
	s_add_i32 s2, s80, s8
	v_mad_i64_i32 v[4:5], s[80:81], v3, s20, v[38:39]
	s_add_i32 s6, s6, s8
	s_mov_b32 s7, s3
	s_lshl_b64 s[80:81], s[2:3], 1
	s_mov_b32 m0, s19
	v_lshl_add_u64 v[6:7], v[4:5], 0, s[80:81]
	s_lshl_b64 s[6:7], s[6:7], 1
	v_cndmask_b32_e64 v3, v113, v112, s[76:77]
	s_waitcnt vmcnt(0) lgkmcnt(0)
	s_barrier
	global_load_lds_dwordx4 v[6:7], off
	v_lshl_add_u64 v[4:5], v[4:5], 0, s[6:7]
	s_mov_b32 m0, s82
	v_add_u32_e32 v3, s84, v3
	global_load_lds_dwordx4 v[4:5], off
	v_mad_i64_i32 v[4:5], s[86:87], v3, s20, v[38:39]
	s_add_i32 s85, s92, 0x1b600
	v_lshl_add_u64 v[6:7], v[4:5], 0, s[80:81]
	s_mov_b32 m0, s85
	s_add_i32 s86, s92, 0x1f600
	global_load_lds_dwordx4 v[6:7], off
	v_lshl_add_u64 v[4:5], v[4:5], 0, s[6:7]
	s_mov_b32 m0, s86
	v_cndmask_b32_e64 v3, v101, v100, s[76:77]
	global_load_lds_dwordx4 v[4:5], off
	v_add_u32_e32 v3, s84, v3
	v_mov_b64_e32 v[4:5], s[26:27]
	s_mov_b32 s79, s3
	v_mad_i64_i32 v[4:5], vcc, v3, s20, v[4:5]
	s_lshl_b64 s[78:79], s[78:79], 1
	s_add_i32 s87, s16, 0
	v_lshl_add_u64 v[4:5], v[4:5], 0, s[78:79]
	v_mov_b32_e32 v45, v195
	s_add_i32 s87, s87, 0x23600
	v_lshl_add_u64 v[4:5], v[4:5], 0, v[44:45]
	s_mov_b32 m0, s87
	v_mul_f32_e32 v144, 0x42800000, v2
	global_load_lds_dwordx4 v[4:5], off
	v_mul_f32_e32 v2, 0x42000000, v2
	v_exp_f32_e32 v18, v2
	s_ashr_i32 s9, s8, 31
	s_waitcnt vmcnt(0)
	s_lshl_b32 s2, s4, 13
	v_mad_i64_i32 v[2:3], s[4:5], s24, v242, v[42:43]
	v_lshl_add_u64 v[2:3], s[8:9], 1, v[2:3]
	s_lshl_b32 s4, s40, 1
	s_mov_b32 s5, s3
	v_mov_b32_e32 v22, 0
	v_lshl_add_u64 v[52:53], v[40:41], 0, s[78:79]
	v_sub_f32_e32 v45, 1.0, v140
	v_sub_f32_e32 v143, 1.0, v139
	v_lshl_add_u64 v[54:55], v[2:3], 0, s[4:5]
	v_mov_b32_e32 v47, v46
	s_mov_b32 s24, 0
	v_mov_b32_e32 v19, v18
	v_mov_b32_e32 v20, v18
	v_mov_b32_e32 v21, v18
	s_mov_b32 s4, 0
	v_mov_b32_e32 v23, v22
	v_mov_b32_e32 v24, v22
	v_mov_b32_e32 v25, v22
	v_mov_b32_e32 v26, v22
	v_mov_b32_e32 v27, v22
	v_mov_b32_e32 v28, v22
	v_mov_b32_e32 v29, v22
	v_mov_b32_e32 v30, v22
	v_mov_b32_e32 v31, v22
	v_mov_b32_e32 v32, v22
	v_mov_b32_e32 v33, v22
	v_mov_b32_e32 v34, v22
	v_mov_b32_e32 v35, v22
	v_mov_b32_e32 v36, v22
	v_mov_b32_e32 v37, v22
	v_add_u32_e32 v177, s24, v118
	v_add_u32_e32 v176, s4, v109
	v_add_u32_e32 v178, 0x7ff, v177
	v_cndmask_b32_e64 v178, v178, v176, s[76:77]
	v_or_b32_e32 v180, s84, v178
	v_ashrrev_i32_e32 v181, 31, v180
	v_lshl_add_u64 v[180:181], v[180:181], 0, s[2:3]
	v_mad_u64_u32 v[192:193], s[8:9], v180, s11, v[54:55]
	v_mad_i32_i24 v193, v181, s11, v193
	v_add_u32_e32 v182, 16, v176
	v_add_u32_e32 v183, 0x7ef, v177
	v_cndmask_b32_e64 v182, v183, v182, s[76:77]
	v_or_b32_e32 v184, s84, v182
	v_ashrrev_i32_e32 v185, 31, v184
	v_lshl_add_u64 v[184:185], v[184:185], 0, s[2:3]
	v_mad_u64_u32 v[216:217], s[8:9], v184, s11, v[54:55]
	v_mad_i32_i24 v217, v185, s11, v217
	v_mov_b32_e32 v186, s11
	v_lshlrev_b32_e32 v186, 6, v186
	v_sub_u32_e32 v187, 0, v186
	v_cndmask_b32_e64 v244, v187, v186, s[76:77]
	v_cndmask_b32_e64 v245, -1, 0, s[76:77]
	s_waitcnt vmcnt(0) lgkmcnt(0)
	s_barrier
	s_branch .LBB0_466
.LBB0_465:
	s_waitcnt lgkmcnt(0)
	s_barrier
	ds_read_b128 v[10:13], v127
	ds_read_b128 v[14:17], v127 offset:64
	ds_read_b128 v[56:59], v127 offset:128
	ds_read_b128 v[60:63], v127 offset:192
	ds_read_b128 v[64:67], v128 offset:17408
	ds_read_b128 v[68:71], v128 offset:17472
	ds_read_b128 v[72:75], v128 offset:17536
	ds_read_b128 v[76:79], v128 offset:17600
	ds_read_b128 v[176:179], v128 offset:21760
	ds_read_b128 v[180:183], v128 offset:21824
	ds_read_b128 v[184:187], v128 offset:21888
	ds_read_b128 v[188:191], v128 offset:21952
	s_waitcnt lgkmcnt(7)
	v_mfma_f32_16x16x32_bf16 v[2:5], v[64:67], v[10:13], 0
	s_waitcnt lgkmcnt(6)
	v_mfma_f32_16x16x32_bf16 v[2:5], v[68:71], v[14:17], v[2:5]
	s_waitcnt lgkmcnt(3)
	v_mfma_f32_16x16x32_bf16 v[6:9], v[176:179], v[10:13], 0
	v_mfma_f32_16x16x32_bf16 v[2:5], v[72:75], v[56:59], v[2:5]
	s_waitcnt lgkmcnt(2)
	v_mfma_f32_16x16x32_bf16 v[6:9], v[180:183], v[14:17], v[6:9]
	v_mfma_f32_16x16x32_bf16 v[2:5], v[76:79], v[60:63], v[2:5]
	s_waitcnt lgkmcnt(1)
	v_mfma_f32_16x16x32_bf16 v[6:9], v[184:187], v[56:59], v[6:9]
	s_waitcnt lgkmcnt(0)
	v_mfma_f32_16x16x32_bf16 v[6:9], v[188:191], v[60:63], v[6:9]
	s_nop 6
	v_cndmask_b32_e64 v56, v2, 0, s[44:45]
	v_cndmask_b32_e64 v57, 0, v3, s[46:47]
	v_cndmask_b32_e64 v58, v4, 0, s[48:49]
	v_cndmask_b32_e64 v59, v5, 0, s[50:51]
	v_cvt_pk_bf16_f32 v56, v56, v57
	v_cvt_pk_bf16_f32 v57, v58, v59
	ds_write_b64 v129, v[56:57]
	v_cndmask_b32_e64 v6, v6, 0, s[52:53]
	v_cndmask_b32_e64 v7, 0, v7, s[54:55]
	v_cndmask_b32_e64 v8, v8, 0, s[56:57]
	v_cndmask_b32_e64 v9, v9, 0, s[58:59]
	v_cvt_pk_bf16_f32 v6, v6, v7
	v_cvt_pk_bf16_f32 v7, v8, v9
	ds_write_b64 v130, v[6:7]
	s_waitcnt lgkmcnt(0)
	s_barrier
	ds_read_b128 v[10:13], v131
	ds_read_b128 v[14:17], v132
	ds_read_b128 v[56:59], v133
	ds_read_b128 v[60:63], v131 offset:64
	ds_read_b128 v[64:67], v132 offset:64
	ds_read_b128 v[68:71], v133 offset:64
	ds_read_b128 v[72:75], v138
	ds_read_b128 v[76:79], v134 offset:52224
	ds_read_b128 v[176:179], v137
	ds_read_b128 v[180:183], v137 offset:2304
	ds_read_b128 v[184:187], v137 offset:4608
	ds_read_b128 v[188:191], v137 offset:6912
	ds_read_b128 v[200:203], v134 offset:52288
	ds_read_b128 v[204:207], v137 offset:64
	ds_read_b128 v[208:211], v137 offset:2368
	s_waitcnt lgkmcnt(13)
	v_mfma_f32_16x16x32_bf16 v[6:9], v[10:13], v[14:17], 0
	s_waitcnt lgkmcnt(12)
	v_mfma_f32_16x16x32_bf16 v[2:5], v[10:13], v[56:59], 0
	ds_read_b128 v[212:215], v137 offset:4672
	ds_read_b128 v[220:223], v137 offset:6976
	ds_read_b128 v[224:227], v135
	s_waitcnt lgkmcnt(13)
	v_mfma_f32_16x16x32_bf16 v[6:9], v[60:63], v[64:67], v[6:9]
	s_waitcnt lgkmcnt(12)
	v_mfma_f32_16x16x32_bf16 v[2:5], v[60:63], v[68:71], v[2:5]
	ds_read_b128 v[232:235], v128
	ds_read_b128 v[236:239], v136
	ds_read_b128 v[14:17], v135 offset:64
	s_waitcnt lgkmcnt(14)
	v_pk_mul_f32 v[22:23], v[22:23], v[72:73]
	v_pk_mul_f32 v[24:25], v[24:25], v[74:75]
	v_pk_mul_f32 v[26:27], v[26:27], v[72:73]
	v_pk_mul_f32 v[28:29], v[28:29], v[74:75]
	v_pk_mul_f32 v[30:31], v[30:31], v[72:73]
	v_pk_mul_f32 v[32:33], v[32:33], v[74:75]
	v_pk_mul_f32 v[34:35], v[34:35], v[72:73]
	v_pk_mul_f32 v[36:37], v[36:37], v[74:75]
	s_waitcnt lgkmcnt(12)
	v_mfma_f32_16x16x32_bf16 v[22:25], v[76:79], v[176:179], v[22:25]
	s_waitcnt lgkmcnt(11)
	v_mfma_f32_16x16x32_bf16 v[26:29], v[76:79], v[180:183], v[26:29]
	s_waitcnt lgkmcnt(10)
	v_mfma_f32_16x16x32_bf16 v[30:33], v[76:79], v[184:187], v[30:33]
	s_waitcnt lgkmcnt(9)
	v_mfma_f32_16x16x32_bf16 v[34:37], v[76:79], v[188:191], v[34:37]
	ds_read_b128 v[10:13], v128 offset:64
	ds_read_b128 v[56:59], v136 offset:64
	ds_read_b128 v[64:67], v135 offset:128
	ds_read_b128 v[60:63], v128 offset:128
	s_waitcnt lgkmcnt(11)
	v_mfma_f32_16x16x32_bf16 v[22:25], v[200:203], v[204:207], v[22:25]
	s_waitcnt lgkmcnt(10)
	v_mfma_f32_16x16x32_bf16 v[26:29], v[200:203], v[208:211], v[26:29]
	ds_read_b128 v[68:71], v136 offset:128
	ds_read_b128 v[72:75], v135 offset:192
	s_waitcnt lgkmcnt(11)
	v_mfma_f32_16x16x32_bf16 v[30:33], v[200:203], v[212:215], v[30:33]
	s_waitcnt lgkmcnt(10)
	v_mfma_f32_16x16x32_bf16 v[34:37], v[200:203], v[220:223], v[34:37]
	ds_read_b128 v[176:179], v128 offset:192
	ds_read_b128 v[180:183], v136 offset:192
	s_waitcnt lgkmcnt(10)
	v_mfma_f32_16x16x32_bf16 v[6:9], v[224:227], v[232:235], v[6:9]
	s_waitcnt lgkmcnt(9)
	v_mfma_f32_16x16x32_bf16 v[2:5], v[224:227], v[236:239], v[2:5]
	s_waitcnt lgkmcnt(7)
	v_mfma_f32_16x16x32_bf16 v[6:9], v[14:17], v[10:13], v[6:9]
	s_waitcnt lgkmcnt(6)
	v_mfma_f32_16x16x32_bf16 v[2:5], v[14:17], v[56:59], v[2:5]
	s_waitcnt lgkmcnt(4)
	v_mfma_f32_16x16x32_bf16 v[6:9], v[64:67], v[60:63], v[6:9]
	s_waitcnt lgkmcnt(3)
	v_mfma_f32_16x16x32_bf16 v[2:5], v[64:67], v[68:71], v[2:5]
	s_waitcnt lgkmcnt(1)
	v_mfma_f32_16x16x32_bf16 v[6:9], v[72:75], v[176:179], v[6:9]
	s_waitcnt lgkmcnt(0)
	v_mfma_f32_16x16x32_bf16 v[2:5], v[72:75], v[180:183], v[2:5]
	s_add_i32 s4, s4, 64
	s_sub_i32 s24, s24, 64
	s_cmpk_eq_i32 s4, 0x800
	s_waitcnt vmcnt(1)
	s_nop 7
	v_cvt_pk_bf16_f32 v6, v6, v7
	v_cvt_pk_bf16_f32 v7, v8, v9
	global_store_dwordx2 v[192:193], v[6:7], off
	v_lshl_add_u64 v[192:193], v[192:193], 0, v[244:245]
	s_nop 3
	v_cvt_pk_bf16_f32 v2, v2, v3
	v_cvt_pk_bf16_f32 v3, v4, v5
	global_store_dwordx2 v[216:217], v[2:3], off
	v_lshl_add_u64 v[216:217], v[216:217], 0, v[244:245]
	s_cbranch_scc1 .LBB0_448
